# mlstm out-unit epilogue: gain loads issued ahead of the previous store as global ops with counted waits
# baseline (speedup 1.0000x reference)
; __device__ __forceinline__ unsigned pk2(float lo, float hi) { const f32x2_t v = {lo, hi}; return __builtin_bit_cast(unsigned, __builtin_convertvector(v, bf16x2_t)); }
; __device__ __forceinline__ float sigmoidf_(float x) { return __builtin_amdgcn_rcpf(1.0f + __expf(-x)); }
; __device__ __forceinline__ void mlstm_out_group(Frame& F, int l, int ug) {
;     ...
;             const float den = __shfl(o[8][0], n);
;             const float dn = 1.0f / fmaxf(fabsf(den), __expf(-(bj + Mj)));
;             float ss = 0.f;
; #pragma unroll
;             for (int mt = 0; mt < 8; ++mt)
; #pragma unroll
;                 for (int r = 0; r < 4; ++r) { o[mt][r] *= dn; ss += o[mt][r] * o[mt][r]; }
;             ss += __shfl_xor(ss, 16); ss += __shfl_xor(ss, 32);
;             const float rstd = 1.0f / sqrtf(ss * (1.0f / 128.0f) + EPS);
; #pragma unroll
;             for (int mt = 0; mt < 8; ++mt) { const int v = 16 * mt + 4 * g;
;                 const f32x4 go4 = *(const f32x4*)(gout + v); const v2u mx = mx8[mt];
;                 v2u wv; wv.x = pk2(o[mt][0] * rstd * go4.x * sigmoidf_(bflo(mx.x)), o[mt][1] * rstd * go4.y * sigmoidf_(bfhi(mx.x))); wv.y = pk2(o[mt][2] * rstd * go4.z * sigmoidf_(bflo(mx.y)), o[mt][3] * rstd * go4.w * sigmoidf_(bfhi(mx.y)));
;                 *(v2u*)(Y + row * DM + h * 128 + v) = wv; }
.LBB0_580:
	s_mov_b32 s26, 0x3fffffc0
	s_nop 5
	v_and_or_b32 v87, v127, s26, v212
	v_lshlrev_b32_e32 v87, 2, v87
	ds_bpermute_b32 v86, v87, v86
	v_add_f32_e32 v87, v152, v153
	v_mul_f32_e32 v87, 0xbfb8aa3b, v87
	v_exp_f32_e32 v87, v87
	v_xor_b32_e32 v88, 16, v127
	s_waitcnt lgkmcnt(0)
	v_max_f32_e64 v86, |v86|, |v86|
	v_add_u32_e32 v89, 64, v118
	v_max_f32_e32 v86, v86, v87
	v_div_scale_f32 v87, s[26:27], v86, v86, 1.0
	v_rcp_f32_e32 v92, v87
	v_cmp_lt_i32_e32 vcc, v88, v89
	v_xor_b32_e32 v90, 32, v127
	v_ashrrev_i32_e32 v151, 31, v150
	v_cndmask_b32_e32 v88, v127, v88, vcc
	v_cmp_lt_i32_e32 vcc, v90, v89
	v_lshlrev_b32_e32 v93, 2, v88
	v_fma_f32 v88, -v87, v92, 1.0
	v_cndmask_b32_e32 v89, v127, v90, vcc
	v_fmac_f32_e32 v92, v88, v92
	v_div_scale_f32 v88, vcc, 1.0, v86, 1.0
	v_lshlrev_b32_e32 v127, 2, v89
	v_mul_f32_e32 v89, v88, v92
	v_fma_f32 v94, -v87, v89, v88
	v_fmac_f32_e32 v89, v94, v92
	v_fma_f32 v87, -v87, v89, v88
	v_div_fmas_f32 v87, v87, v92, v89
	s_add_u32 s24, s88, s70
	v_div_fixup_f32 v136, v87, v86, 1.0
	s_addc_u32 s25, s89, 0
	v_lshlrev_b64 v[90:91], 12, v[150:151]
	v_pk_mul_f32 v[88:89], v[28:29], v[136:137] op_sel_hi:[1,0]
	v_pk_mul_f32 v[28:29], v[46:47], v[136:137] op_sel_hi:[1,0]
	s_waitcnt vmcnt(0)
	v_lshlrev_b32_e32 v46, 16, v116
	v_lshlrev_b32_e32 v118, 2, v124
	v_lshl_add_u64 v[94:95], s[24:25], 0, v[90:91]
	v_mul_f32_e32 v46, 0xbfb8aa3b, v46
	v_lshl_add_u64 v[90:91], s[62:63], 0, v[118:119]
	v_pk_mul_f32 v[86:87], v[48:49], v[136:137] op_sel_hi:[1,0]
	v_exp_f32_e32 v92, v46
	global_load_dwordx4 v[46:49], v[90:91], off
	v_pk_mul_f32 v[100:101], v[42:43], v[136:137] op_sel_hi:[1,0]
	v_pk_mul_f32 v[44:45], v[44:45], v[136:137] op_sel_hi:[1,0]
	v_pk_mul_f32 v[180:181], v[100:101], v[100:101]
	v_pk_mul_f32 v[178:179], v[44:45], v[44:45]
	v_add_f32_e32 v118, v180, v181
	v_and_b32_e32 v96, 0xffff0000, v116
	v_pk_mul_f32 v[184:185], v[38:39], v[136:137] op_sel_hi:[1,0]
	v_add_f32_e32 v118, v178, v118
	v_mul_f32_e32 v96, 0xbfb8aa3b, v96
	v_pk_mul_f32 v[190:191], v[184:185], v[184:185]
	v_add_f32_e32 v118, v179, v118
	v_exp_f32_e32 v116, v96
	v_pk_mul_f32 v[96:97], v[40:41], v[136:137] op_sel_hi:[1,0]
	v_add_f32_e32 v118, v190, v118
	v_pk_mul_f32 v[182:183], v[96:97], v[96:97]
	v_add_f32_e32 v118, v191, v118
	v_pk_mul_f32 v[98:99], v[30:31], v[136:137] op_sel_hi:[1,0]
	v_add_f32_e32 v118, v182, v118
	v_pk_mul_f32 v[194:195], v[98:99], v[98:99]
	v_add_f32_e32 v118, v183, v118
	v_pk_mul_f32 v[42:43], v[32:33], v[136:137] op_sel_hi:[1,0]
	v_add_f32_e32 v118, v194, v118
	v_pk_mul_f32 v[192:193], v[42:43], v[42:43]
	v_add_f32_e32 v118, v195, v118
	v_pk_mul_f32 v[40:41], v[18:19], v[136:137] op_sel_hi:[1,0]
	v_add_f32_e32 v118, v192, v118
	v_pk_mul_f32 v[18:19], v[40:41], v[40:41]
	v_add_f32_e32 v118, v193, v118
	v_pk_mul_f32 v[38:39], v[20:21], v[136:137] op_sel_hi:[1,0]
	v_add_f32_e32 v18, v18, v118
	v_pk_mul_f32 v[196:197], v[38:39], v[38:39]
	v_add_f32_e32 v18, v19, v18
	v_pk_mul_f32 v[34:35], v[34:35], v[136:137] op_sel_hi:[1,0]
	v_add_f32_e32 v18, v196, v18
	v_pk_mul_f32 v[198:199], v[34:35], v[34:35]
	v_add_f32_e32 v18, v197, v18
	v_pk_mul_f32 v[32:33], v[36:37], v[136:137] op_sel_hi:[1,0]
	v_add_f32_e32 v18, v198, v18
	v_pk_mul_f32 v[36:37], v[32:33], v[32:33]
	v_add_f32_e32 v18, v199, v18
	v_pk_mul_f32 v[30:31], v[22:23], v[136:137] op_sel_hi:[1,0]
	v_add_f32_e32 v18, v36, v18
	v_pk_mul_f32 v[22:23], v[30:31], v[30:31]
	v_add_f32_e32 v18, v37, v18
	v_pk_mul_f32 v[24:25], v[24:25], v[136:137] op_sel_hi:[1,0]
	v_add_f32_e32 v18, v22, v18
	v_pk_mul_f32 v[200:201], v[24:25], v[24:25]
	v_add_f32_e32 v18, v23, v18
	v_pk_mul_f32 v[20:21], v[26:27], v[136:137] op_sel_hi:[1,0]
	v_add_f32_e32 v18, v200, v18
	v_pk_mul_f32 v[26:27], v[20:21], v[20:21]
	v_add_f32_e32 v18, v201, v18
	v_add_f32_e32 v18, v26, v18
	v_pk_mul_f32 v[150:151], v[88:89], v[88:89]
	v_add_f32_e32 v18, v27, v18
	v_add_f32_e32 v18, v150, v18
	v_pk_mul_f32 v[152:153], v[28:29], v[28:29]
	v_add_f32_e32 v18, v151, v18
	v_add_f32_e32 v18, v152, v18
	v_pk_mul_f32 v[176:177], v[86:87], v[86:87]
	v_add_f32_e32 v18, v153, v18
	v_add_f32_e32 v18, v176, v18
	v_add_f32_e32 v18, v177, v18
	ds_bpermute_b32 v19, v93, v18
	v_add_f32_e32 v22, 1.0, v116
	v_rcp_f32_e32 v93, v22
	v_lshlrev_b32_e32 v22, 16, v117
	s_mov_b32 s24, 0xf800000
	s_waitcnt lgkmcnt(0)
	v_add_f32_e32 v18, v18, v19
	ds_bpermute_b32 v19, v127, v18
	v_mul_f32_e32 v22, 0xbfb8aa3b, v22
	v_and_b32_e32 v23, 0xffff0000, v117
	v_exp_f32_e32 v22, v22
	v_mul_f32_e32 v23, 0xbfb8aa3b, v23
	s_waitcnt lgkmcnt(0)
	v_add_f32_e32 v18, v18, v19
	v_fmamk_f32 v18, v18, 0x3c000000, v170
	v_mul_f32_e32 v19, 0x4f800000, v18
	v_cmp_gt_f32_e32 vcc, s24, v18
	v_exp_f32_e32 v23, v23
	v_add_f32_e32 v22, 1.0, v22
	v_cndmask_b32_e32 v18, v18, v19, vcc
	v_sqrt_f32_e32 v19, v18
	v_rcp_f32_e32 v26, v22
	v_add_f32_e32 v22, 1.0, v23
	v_mov_b32_e32 v133, v119
	v_add_u32_e32 v23, -1, v19
	v_fma_f32 v27, -v23, v19, v18
	v_cmp_ge_f32_e64 s[24:25], 0, v27
	v_add_u32_e32 v27, 1, v19
	v_add_f32_e32 v92, 1.0, v92
	v_cndmask_b32_e64 v23, v19, v23, s[24:25]
	v_fma_f32 v19, -v27, v19, v18
	v_cmp_lt_f32_e64 s[24:25], 0, v19
	v_rcp_f32_e32 v92, v92
	s_nop 0
	v_cndmask_b32_e64 v19, v23, v27, s[24:25]
	v_mul_f32_e32 v23, 0x37800000, v19
	v_cndmask_b32_e32 v19, v19, v23, vcc
	v_cmp_class_f32_e32 vcc, v18, v171
	v_rcp_f32_e32 v27, v22
	s_nop 0
	v_cndmask_b32_e32 v23, v19, v18, vcc
	v_div_scale_f32 v36, s[24:25], v23, v23, 1.0
	v_rcp_f32_e32 v37, v36
	v_lshl_add_u64 v[18:19], v[94:95], 0, v[132:133]
	s_mov_b64 s[24:25], 0
	v_fma_f32 v22, -v36, v37, 1.0
	v_fmac_f32_e32 v37, v22, v37
	v_div_scale_f32 v22, vcc, 1.0, v23, 1.0
	v_mul_f32_e32 v94, v22, v37
	v_fma_f32 v95, -v36, v94, v22
	v_fmac_f32_e32 v94, v95, v37
	v_fma_f32 v22, -v36, v94, v22
	v_div_fmas_f32 v22, v22, v37, v94
	v_div_fixup_f32 v22, v22, v23, 1.0
	v_pk_mul_f32 v[36:37], v[100:101], v[22:23] op_sel_hi:[1,0]
	v_pk_mul_f32 v[44:45], v[44:45], v[22:23] op_sel_hi:[1,0]
	s_waitcnt vmcnt(0)
; __device__ __forceinline__ unsigned pk2(float lo, float hi) { const f32x2_t v = {lo, hi}; return __builtin_bit_cast(unsigned, __builtin_convertvector(v, bf16x2_t)); }
; __device__ __forceinline__ float sigmoidf_(float x) { return __builtin_amdgcn_rcpf(1.0f + __expf(-x)); }
; __device__ __forceinline__ void mlstm_out_group(Frame& F, int l, int ug) {
;     ...
; #pragma unroll
;             for (int mt = 0; mt < 8; ++mt) { const int v = 16 * mt + 4 * g;
;                 const f32x4 go4 = *(const f32x4*)(gout + v); const v2u mx = mx8[mt];
;                 v2u wv; wv.x = pk2(o[mt][0] * rstd * go4.x * sigmoidf_(bflo(mx.x)), o[mt][1] * rstd * go4.y * sigmoidf_(bfhi(mx.x))); wv.y = pk2(o[mt][2] * rstd * go4.z * sigmoidf_(bflo(mx.y)), o[mt][3] * rstd * go4.w * sigmoidf_(bfhi(mx.y)));
;                 *(v2u*)(Y + row * DM + h * 128 + v) = wv; }
	v_pk_mul_f32 v[36:37], v[46:47], v[36:37]
	v_pk_mul_f32 v[44:45], v[48:49], v[44:45]
	v_pk_mul_f32 v[36:37], v[92:93], v[36:37]
	v_pk_mul_f32 v[26:27], v[26:27], v[44:45]
	v_cvt_pk_bf16_f32 v36, v36, v37
	v_cvt_pk_bf16_f32 v37, v26, v27
	global_load_dwordx4 v[44:47], v[90:91], off offset:64
	global_store_dwordx2 v[18:19], v[36:37], off
	v_lshlrev_b32_e32 v23, 16, v114
	v_mul_f32_e32 v23, 0xbfb8aa3b, v23
	v_and_b32_e32 v26, 0xffff0000, v114
	v_exp_f32_e32 v23, v23
	v_mul_f32_e32 v26, 0xbfb8aa3b, v26
	v_exp_f32_e32 v27, v26
	s_andn2_b64 vcc, exec, s[90:91]
	v_add_f32_e32 v23, 1.0, v23
	v_rcp_f32_e32 v26, v23
	v_add_f32_e32 v23, 1.0, v27
	v_lshlrev_b32_e32 v27, 16, v115
	v_mul_f32_e32 v27, 0xbfb8aa3b, v27
	v_exp_f32_e32 v36, v27
	v_and_b32_e32 v27, 0xffff0000, v115
	v_mul_f32_e32 v27, 0xbfb8aa3b, v27
	v_exp_f32_e32 v37, v27
	v_rcp_f32_e32 v27, v23
	v_add_f32_e32 v23, 1.0, v36
	v_rcp_f32_e32 v36, v23
	v_add_f32_e32 v23, 1.0, v37
	v_rcp_f32_e32 v37, v23
	v_pk_mul_f32 v[48:49], v[184:185], v[22:23] op_sel_hi:[1,0]
	s_waitcnt vmcnt(1) lgkmcnt(0)
	v_pk_mul_f32 v[44:45], v[44:45], v[48:49]
	s_nop 0
	v_pk_mul_f32 v[26:27], v[26:27], v[44:45]
	v_pk_mul_f32 v[44:45], v[96:97], v[22:23] op_sel_hi:[1,0]
	v_cvt_pk_bf16_f32 v26, v26, v27
	v_pk_mul_f32 v[44:45], v[46:47], v[44:45]
	v_lshlrev_b32_e32 v23, 16, v112
	v_pk_mul_f32 v[36:37], v[36:37], v[44:45]
	v_mul_f32_e32 v23, 0xbfb8aa3b, v23
	v_cvt_pk_bf16_f32 v27, v36, v37
	global_load_dwordx4 v[44:47], v[90:91], off offset:128
	global_store_dwordx2 v[18:19], v[26:27], off offset:32
	v_and_b32_e32 v26, 0xffff0000, v112
	v_lshlrev_b32_e32 v27, 16, v113
	v_and_b32_e32 v36, 0xffff0000, v113
	v_mul_f32_e32 v26, 0xbfb8aa3b, v26
	v_mul_f32_e32 v27, 0xbfb8aa3b, v27
	v_mul_f32_e32 v36, 0xbfb8aa3b, v36
	v_exp_f32_e32 v23, v23
	v_exp_f32_e32 v26, v26
	v_exp_f32_e32 v27, v27
	v_exp_f32_e32 v36, v36
	v_add_f32_e32 v23, 1.0, v23
	v_add_f32_e32 v37, 1.0, v26
	v_add_f32_e32 v48, 1.0, v27
	v_add_f32_e32 v49, 1.0, v36
	v_rcp_f32_e32 v26, v23
	v_rcp_f32_e32 v27, v37
	v_rcp_f32_e32 v36, v48
	v_rcp_f32_e32 v37, v49
	v_pk_mul_f32 v[48:49], v[98:99], v[22:23] op_sel_hi:[1,0]
	v_pk_mul_f32 v[42:43], v[42:43], v[22:23] op_sel_hi:[1,0]
	v_lshlrev_b32_e32 v23, 16, v110
	v_mul_f32_e32 v23, 0xbfb8aa3b, v23
	v_exp_f32_e32 v23, v23
	s_waitcnt vmcnt(1) lgkmcnt(0)
	v_pk_mul_f32 v[44:45], v[44:45], v[48:49]
	v_pk_mul_f32 v[42:43], v[46:47], v[42:43]
	v_pk_mul_f32 v[26:27], v[26:27], v[44:45]
	v_pk_mul_f32 v[36:37], v[36:37], v[42:43]
	v_cvt_pk_bf16_f32 v26, v26, v27
	v_cvt_pk_bf16_f32 v27, v36, v37
	global_load_dwordx4 v[42:45], v[90:91], off offset:192
	global_store_dwordx2 v[18:19], v[26:27], off offset:64
	v_and_b32_e32 v26, 0xffff0000, v110
	v_lshlrev_b32_e32 v27, 16, v111
	v_and_b32_e32 v36, 0xffff0000, v111
	v_mul_f32_e32 v26, 0xbfb8aa3b, v26
	v_mul_f32_e32 v27, 0xbfb8aa3b, v27
	v_mul_f32_e32 v36, 0xbfb8aa3b, v36
	v_exp_f32_e32 v26, v26
	v_exp_f32_e32 v27, v27
	v_exp_f32_e32 v36, v36
	v_add_f32_e32 v23, 1.0, v23
	v_add_f32_e32 v37, 1.0, v26
	v_add_f32_e32 v46, 1.0, v27
	v_add_f32_e32 v47, 1.0, v36
	v_rcp_f32_e32 v26, v23
	v_rcp_f32_e32 v27, v37
	v_rcp_f32_e32 v36, v46
	v_rcp_f32_e32 v37, v47
	v_pk_mul_f32 v[40:41], v[40:41], v[22:23] op_sel_hi:[1,0]
	v_pk_mul_f32 v[38:39], v[38:39], v[22:23] op_sel_hi:[1,0]
	v_lshlrev_b32_e32 v23, 16, v108
	v_mul_f32_e32 v23, 0xbfb8aa3b, v23
	v_exp_f32_e32 v23, v23
	s_waitcnt vmcnt(1) lgkmcnt(0)
	v_pk_mul_f32 v[40:41], v[42:43], v[40:41]
	v_pk_mul_f32 v[38:39], v[44:45], v[38:39]
	v_pk_mul_f32 v[26:27], v[26:27], v[40:41]
	v_pk_mul_f32 v[36:37], v[36:37], v[38:39]
	v_cvt_pk_bf16_f32 v26, v26, v27
	v_cvt_pk_bf16_f32 v27, v36, v37
	global_load_dwordx4 v[36:39], v[90:91], off offset:256
	global_store_dwordx2 v[18:19], v[26:27], off offset:96
	v_and_b32_e32 v26, 0xffff0000, v108
	v_lshlrev_b32_e32 v27, 16, v109
	v_and_b32_e32 v40, 0xffff0000, v109
	v_mul_f32_e32 v26, 0xbfb8aa3b, v26
	v_mul_f32_e32 v27, 0xbfb8aa3b, v27
	v_mul_f32_e32 v40, 0xbfb8aa3b, v40
	v_exp_f32_e32 v26, v26
	v_exp_f32_e32 v27, v27
	v_exp_f32_e32 v40, v40
	v_add_f32_e32 v23, 1.0, v23
	v_add_f32_e32 v41, 1.0, v26
	v_add_f32_e32 v42, 1.0, v27
	v_add_f32_e32 v43, 1.0, v40
	v_rcp_f32_e32 v26, v23
	v_rcp_f32_e32 v27, v41
	v_rcp_f32_e32 v40, v42
	v_rcp_f32_e32 v41, v43
	v_pk_mul_f32 v[34:35], v[34:35], v[22:23] op_sel_hi:[1,0]
	v_pk_mul_f32 v[32:33], v[32:33], v[22:23] op_sel_hi:[1,0]
	v_lshlrev_b32_e32 v23, 16, v106
	v_mul_f32_e32 v23, 0xbfb8aa3b, v23
	v_exp_f32_e32 v23, v23
	s_waitcnt vmcnt(1) lgkmcnt(0)
; __device__ __forceinline__ unsigned pk2(float lo, float hi) { const f32x2_t v = {lo, hi}; return __builtin_bit_cast(unsigned, __builtin_convertvector(v, bf16x2_t)); }
; __device__ __forceinline__ float sigmoidf_(float x) { return __builtin_amdgcn_rcpf(1.0f + __expf(-x)); }
; __device__ __forceinline__ void mlstm_out_group(Frame& F, int l, int ug) {
;     ...
; #pragma unroll
;             for (int mt = 0; mt < 8; ++mt) { const int v = 16 * mt + 4 * g;
;                 const f32x4 go4 = *(const f32x4*)(gout + v); const v2u mx = mx8[mt];
;                 v2u wv; wv.x = pk2(o[mt][0] * rstd * go4.x * sigmoidf_(bflo(mx.x)), o[mt][1] * rstd * go4.y * sigmoidf_(bfhi(mx.x))); wv.y = pk2(o[mt][2] * rstd * go4.z * sigmoidf_(bflo(mx.y)), o[mt][3] * rstd * go4.w * sigmoidf_(bfhi(mx.y)));
;                 *(v2u*)(Y + row * DM + h * 128 + v) = wv; }
	v_pk_mul_f32 v[34:35], v[36:37], v[34:35]
	v_pk_mul_f32 v[32:33], v[38:39], v[32:33]
	v_pk_mul_f32 v[26:27], v[26:27], v[34:35]
	v_pk_mul_f32 v[32:33], v[40:41], v[32:33]
	v_cvt_pk_bf16_f32 v26, v26, v27
	v_cvt_pk_bf16_f32 v27, v32, v33
	global_load_dwordx4 v[32:35], v[90:91], off offset:320
	global_store_dwordx2 v[18:19], v[26:27], off offset:128
	v_and_b32_e32 v26, 0xffff0000, v106
	v_lshlrev_b32_e32 v27, 16, v107
	v_and_b32_e32 v36, 0xffff0000, v107
	v_mul_f32_e32 v26, 0xbfb8aa3b, v26
	v_mul_f32_e32 v27, 0xbfb8aa3b, v27
	v_mul_f32_e32 v36, 0xbfb8aa3b, v36
	v_exp_f32_e32 v26, v26
	v_exp_f32_e32 v27, v27
	v_exp_f32_e32 v36, v36
	v_add_f32_e32 v23, 1.0, v23
	v_add_f32_e32 v37, 1.0, v26
	v_add_f32_e32 v38, 1.0, v27
	v_add_f32_e32 v39, 1.0, v36
	v_rcp_f32_e32 v26, v23
	v_rcp_f32_e32 v27, v37
	v_rcp_f32_e32 v36, v38
	v_rcp_f32_e32 v37, v39
	v_pk_mul_f32 v[30:31], v[30:31], v[22:23] op_sel_hi:[1,0]
	v_pk_mul_f32 v[24:25], v[24:25], v[22:23] op_sel_hi:[1,0]
	v_lshlrev_b32_e32 v23, 16, v104
	v_mul_f32_e32 v23, 0xbfb8aa3b, v23
	v_exp_f32_e32 v23, v23
	s_waitcnt vmcnt(1) lgkmcnt(0)
	v_pk_mul_f32 v[30:31], v[32:33], v[30:31]
	v_pk_mul_f32 v[24:25], v[34:35], v[24:25]
	v_pk_mul_f32 v[26:27], v[26:27], v[30:31]
	v_pk_mul_f32 v[24:25], v[36:37], v[24:25]
	v_cvt_pk_bf16_f32 v26, v26, v27
	v_cvt_pk_bf16_f32 v27, v24, v25
	global_store_dwordx2 v[18:19], v[26:27], off offset:160
	global_load_dwordx4 v[24:27], v[90:91], off offset:384
	v_and_b32_e32 v30, 0xffff0000, v104
	v_lshlrev_b32_e32 v31, 16, v105
	v_and_b32_e32 v32, 0xffff0000, v105
	v_mul_f32_e32 v30, 0xbfb8aa3b, v30
	v_mul_f32_e32 v31, 0xbfb8aa3b, v31
	v_mul_f32_e32 v32, 0xbfb8aa3b, v32
	v_exp_f32_e32 v30, v30
	v_exp_f32_e32 v31, v31
	v_exp_f32_e32 v32, v32
	v_add_f32_e32 v23, 1.0, v23
	v_add_f32_e32 v33, 1.0, v30
	v_add_f32_e32 v34, 1.0, v31
	v_add_f32_e32 v35, 1.0, v32
	v_rcp_f32_e32 v30, v23
	v_rcp_f32_e32 v31, v33
	v_rcp_f32_e32 v32, v34
	v_rcp_f32_e32 v33, v35
	v_pk_mul_f32 v[20:21], v[20:21], v[22:23] op_sel_hi:[1,0]
	v_pk_mul_f32 v[34:35], v[88:89], v[22:23] op_sel_hi:[1,0]
	v_lshlrev_b32_e32 v23, 16, v103
	v_mul_f32_e32 v23, 0xbfb8aa3b, v23
	v_exp_f32_e32 v23, v23
	s_waitcnt vmcnt(0) lgkmcnt(0)
	v_pk_mul_f32 v[20:21], v[24:25], v[20:21]
	v_pk_mul_f32 v[24:25], v[26:27], v[34:35]
	v_pk_mul_f32 v[20:21], v[30:31], v[20:21]
	v_pk_mul_f32 v[24:25], v[32:33], v[24:25]
	v_cvt_pk_bf16_f32 v20, v20, v21
	v_cvt_pk_bf16_f32 v21, v24, v25
	global_load_dwordx4 v[24:27], v[90:91], off offset:448
	global_store_dwordx2 v[18:19], v[20:21], off offset:192
	v_lshlrev_b32_e32 v20, 16, v102
	v_and_b32_e32 v21, 0xffff0000, v102
	v_and_b32_e32 v30, 0xffff0000, v103
	v_mul_f32_e32 v20, 0xbfb8aa3b, v20
	v_mul_f32_e32 v21, 0xbfb8aa3b, v21
	v_mul_f32_e32 v30, 0xbfb8aa3b, v30
	v_exp_f32_e32 v20, v20
	v_exp_f32_e32 v21, v21
	v_exp_f32_e32 v30, v30
	v_add_f32_e32 v23, 1.0, v23
	v_add_f32_e32 v20, 1.0, v20
	v_add_f32_e32 v21, 1.0, v21
	v_add_f32_e32 v31, 1.0, v30
	v_rcp_f32_e32 v20, v20
	v_rcp_f32_e32 v21, v21
	v_rcp_f32_e32 v30, v23
	v_rcp_f32_e32 v31, v31
	v_pk_mul_f32 v[28:29], v[28:29], v[22:23] op_sel_hi:[1,0]
	v_pk_mul_f32 v[22:23], v[86:87], v[22:23] op_sel_hi:[1,0]
	s_waitcnt vmcnt(1) lgkmcnt(0)
	v_pk_mul_f32 v[24:25], v[24:25], v[28:29]
	v_pk_mul_f32 v[22:23], v[26:27], v[22:23]
	v_pk_mul_f32 v[20:21], v[20:21], v[24:25]
	v_pk_mul_f32 v[22:23], v[30:31], v[22:23]
	v_cvt_pk_bf16_f32 v20, v20, v21
	v_cvt_pk_bf16_f32 v21, v22, v23
	global_store_dwordx2 v[18:19], v[20:21], off offset:224
	s_cbranch_vccz .LBB0_578

; __device__ __forceinline__ unsigned pk2(float lo, float hi) { const f32x2_t v = {lo, hi}; return __builtin_bit_cast(unsigned, __builtin_convertvector(v, bf16x2_t)); }
; __device__ __forceinline__ float sigmoidf_(float x) { return __builtin_amdgcn_rcpf(1.0f + __expf(-x)); }
; __device__ __forceinline__ void mlstm_out_group(Frame& F, int l, int ug) {
;     ...
;             const float den = __shfl(o[8][0], n);
;             const float dn = 1.0f / fmaxf(fabsf(den), __expf(-(bj + Mj)));
;             float ss = 0.f;
; #pragma unroll
;             for (int mt = 0; mt < 8; ++mt)
; #pragma unroll
;                 for (int r = 0; r < 4; ++r) { o[mt][r] *= dn; ss += o[mt][r] * o[mt][r]; }
;             ss += __shfl_xor(ss, 16); ss += __shfl_xor(ss, 32);
;             const float rstd = 1.0f / sqrtf(ss * (1.0f / 128.0f) + EPS);
; #pragma unroll
;             for (int mt = 0; mt < 8; ++mt) { const int v = 16 * mt + 4 * g;
;                 const f32x4 go4 = *(const f32x4*)(gout + v); const v2u mx = mx8[mt];
;                 v2u wv; wv.x = pk2(o[mt][0] * rstd * go4.x * sigmoidf_(bflo(mx.x)), o[mt][1] * rstd * go4.y * sigmoidf_(bfhi(mx.x))); wv.y = pk2(o[mt][2] * rstd * go4.z * sigmoidf_(bflo(mx.y)), o[mt][3] * rstd * go4.w * sigmoidf_(bfhi(mx.y)));
;                 *(v2u*)(Y + row * DM + h * 128 + v) = wv; }
.LBB0_1289:
	s_mov_b32 s26, 0x3fffffc0
	s_nop 5
	v_and_or_b32 v87, v127, s26, v212
	v_lshlrev_b32_e32 v87, 2, v87
	ds_bpermute_b32 v86, v87, v86
	v_add_f32_e32 v87, v152, v153
	v_mul_f32_e32 v87, 0xbfb8aa3b, v87
	v_exp_f32_e32 v87, v87
	v_xor_b32_e32 v88, 16, v127
	s_waitcnt lgkmcnt(0)
	v_max_f32_e64 v86, |v86|, |v86|
	v_add_u32_e32 v89, 64, v118
	v_max_f32_e32 v86, v86, v87
	v_div_scale_f32 v87, s[26:27], v86, v86, 1.0
	v_rcp_f32_e32 v92, v87
	v_cmp_lt_i32_e32 vcc, v88, v89
	v_xor_b32_e32 v90, 32, v127
	v_ashrrev_i32_e32 v151, 31, v150
	v_cndmask_b32_e32 v88, v127, v88, vcc
	v_cmp_lt_i32_e32 vcc, v90, v89
	v_lshlrev_b32_e32 v93, 2, v88
	v_fma_f32 v88, -v87, v92, 1.0
	v_cndmask_b32_e32 v89, v127, v90, vcc
	v_fmac_f32_e32 v92, v88, v92
	v_div_scale_f32 v88, vcc, 1.0, v86, 1.0
	v_lshlrev_b32_e32 v127, 2, v89
	v_mul_f32_e32 v89, v88, v92
	v_fma_f32 v94, -v87, v89, v88
	v_fmac_f32_e32 v89, v94, v92
	v_fma_f32 v87, -v87, v89, v88
	v_div_fmas_f32 v87, v87, v92, v89
	s_add_u32 s24, s36, s66
	v_div_fixup_f32 v136, v87, v86, 1.0
	s_addc_u32 s25, s37, 0
	v_lshlrev_b64 v[90:91], 12, v[150:151]
	v_pk_mul_f32 v[88:89], v[28:29], v[136:137] op_sel_hi:[1,0]
	v_pk_mul_f32 v[28:29], v[46:47], v[136:137] op_sel_hi:[1,0]
	s_waitcnt vmcnt(0)
	v_lshlrev_b32_e32 v46, 16, v116
	v_lshlrev_b32_e32 v118, 2, v124
	v_lshl_add_u64 v[94:95], s[24:25], 0, v[90:91]
	v_mul_f32_e32 v46, 0xbfb8aa3b, v46
	v_lshl_add_u64 v[90:91], s[94:95], 0, v[118:119]
	v_pk_mul_f32 v[86:87], v[48:49], v[136:137] op_sel_hi:[1,0]
	v_exp_f32_e32 v92, v46
	global_load_dwordx4 v[46:49], v[90:91], off
	v_pk_mul_f32 v[100:101], v[42:43], v[136:137] op_sel_hi:[1,0]
	v_pk_mul_f32 v[44:45], v[44:45], v[136:137] op_sel_hi:[1,0]
	v_pk_mul_f32 v[180:181], v[100:101], v[100:101]
	v_pk_mul_f32 v[178:179], v[44:45], v[44:45]
	v_add_f32_e32 v118, v180, v181
	v_and_b32_e32 v96, 0xffff0000, v116
	v_pk_mul_f32 v[184:185], v[38:39], v[136:137] op_sel_hi:[1,0]
	v_add_f32_e32 v118, v178, v118
	v_mul_f32_e32 v96, 0xbfb8aa3b, v96
	v_pk_mul_f32 v[190:191], v[184:185], v[184:185]
	v_add_f32_e32 v118, v179, v118
	v_exp_f32_e32 v116, v96
	v_pk_mul_f32 v[96:97], v[40:41], v[136:137] op_sel_hi:[1,0]
	v_add_f32_e32 v118, v190, v118
	v_pk_mul_f32 v[182:183], v[96:97], v[96:97]
	v_add_f32_e32 v118, v191, v118
	v_pk_mul_f32 v[98:99], v[30:31], v[136:137] op_sel_hi:[1,0]
	v_add_f32_e32 v118, v182, v118
	v_pk_mul_f32 v[194:195], v[98:99], v[98:99]
	v_add_f32_e32 v118, v183, v118
	v_pk_mul_f32 v[42:43], v[32:33], v[136:137] op_sel_hi:[1,0]
	v_add_f32_e32 v118, v194, v118
	v_pk_mul_f32 v[192:193], v[42:43], v[42:43]
	v_add_f32_e32 v118, v195, v118
	v_pk_mul_f32 v[40:41], v[18:19], v[136:137] op_sel_hi:[1,0]
	v_add_f32_e32 v118, v192, v118
	v_pk_mul_f32 v[18:19], v[40:41], v[40:41]
	v_add_f32_e32 v118, v193, v118
	v_pk_mul_f32 v[38:39], v[20:21], v[136:137] op_sel_hi:[1,0]
	v_add_f32_e32 v18, v18, v118
	v_pk_mul_f32 v[196:197], v[38:39], v[38:39]
	v_add_f32_e32 v18, v19, v18
	v_pk_mul_f32 v[34:35], v[34:35], v[136:137] op_sel_hi:[1,0]
	v_add_f32_e32 v18, v196, v18
	v_pk_mul_f32 v[198:199], v[34:35], v[34:35]
	v_add_f32_e32 v18, v197, v18
	v_pk_mul_f32 v[32:33], v[36:37], v[136:137] op_sel_hi:[1,0]
	v_add_f32_e32 v18, v198, v18
	v_pk_mul_f32 v[36:37], v[32:33], v[32:33]
	v_add_f32_e32 v18, v199, v18
	v_pk_mul_f32 v[30:31], v[22:23], v[136:137] op_sel_hi:[1,0]
	v_add_f32_e32 v18, v36, v18
	v_pk_mul_f32 v[22:23], v[30:31], v[30:31]
	v_add_f32_e32 v18, v37, v18
	v_pk_mul_f32 v[24:25], v[24:25], v[136:137] op_sel_hi:[1,0]
	v_add_f32_e32 v18, v22, v18
	v_pk_mul_f32 v[200:201], v[24:25], v[24:25]
	v_add_f32_e32 v18, v23, v18
	v_pk_mul_f32 v[20:21], v[26:27], v[136:137] op_sel_hi:[1,0]
	v_add_f32_e32 v18, v200, v18
	v_pk_mul_f32 v[26:27], v[20:21], v[20:21]
	v_add_f32_e32 v18, v201, v18
	v_add_f32_e32 v18, v26, v18
	v_pk_mul_f32 v[150:151], v[88:89], v[88:89]
	v_add_f32_e32 v18, v27, v18
	v_add_f32_e32 v18, v150, v18
	v_pk_mul_f32 v[152:153], v[28:29], v[28:29]
	v_add_f32_e32 v18, v151, v18
	v_add_f32_e32 v18, v152, v18
	v_pk_mul_f32 v[176:177], v[86:87], v[86:87]
	v_add_f32_e32 v18, v153, v18
	v_add_f32_e32 v18, v176, v18
	v_add_f32_e32 v18, v177, v18
	ds_bpermute_b32 v19, v93, v18
	v_add_f32_e32 v22, 1.0, v116
	v_rcp_f32_e32 v93, v22
	v_lshlrev_b32_e32 v22, 16, v117
	s_mov_b32 s24, 0xf800000
	s_waitcnt lgkmcnt(0)
	v_add_f32_e32 v18, v18, v19
	ds_bpermute_b32 v19, v127, v18
	v_mul_f32_e32 v22, 0xbfb8aa3b, v22
	v_and_b32_e32 v23, 0xffff0000, v117
	v_exp_f32_e32 v22, v22
	v_mul_f32_e32 v23, 0xbfb8aa3b, v23
	s_waitcnt lgkmcnt(0)
	v_add_f32_e32 v18, v18, v19
	v_fmamk_f32 v18, v18, 0x3c000000, v170
	v_mul_f32_e32 v19, 0x4f800000, v18
	v_cmp_gt_f32_e32 vcc, s24, v18
	v_exp_f32_e32 v23, v23
	v_add_f32_e32 v22, 1.0, v22
	v_cndmask_b32_e32 v18, v18, v19, vcc
	v_sqrt_f32_e32 v19, v18
	v_rcp_f32_e32 v26, v22
	v_add_f32_e32 v22, 1.0, v23
	v_mov_b32_e32 v133, v119
	v_add_u32_e32 v23, -1, v19
	v_fma_f32 v27, -v23, v19, v18
	v_cmp_ge_f32_e64 s[24:25], 0, v27
	v_add_u32_e32 v27, 1, v19
	v_add_f32_e32 v92, 1.0, v92
	v_cndmask_b32_e64 v23, v19, v23, s[24:25]
	v_fma_f32 v19, -v27, v19, v18
	v_cmp_lt_f32_e64 s[24:25], 0, v19
	v_rcp_f32_e32 v92, v92
	s_nop 0
	v_cndmask_b32_e64 v19, v23, v27, s[24:25]
	v_mul_f32_e32 v23, 0x37800000, v19
	v_cndmask_b32_e32 v19, v19, v23, vcc
	v_cmp_class_f32_e32 vcc, v18, v171
	v_rcp_f32_e32 v27, v22
	s_nop 0
	v_cndmask_b32_e32 v23, v19, v18, vcc
	v_div_scale_f32 v36, s[24:25], v23, v23, 1.0
	v_rcp_f32_e32 v37, v36
	v_lshl_add_u64 v[18:19], v[94:95], 0, v[132:133]
	s_mov_b64 s[24:25], 0
	v_fma_f32 v22, -v36, v37, 1.0
	v_fmac_f32_e32 v37, v22, v37
	v_div_scale_f32 v22, vcc, 1.0, v23, 1.0
	v_mul_f32_e32 v94, v22, v37
	v_fma_f32 v95, -v36, v94, v22
	v_fmac_f32_e32 v94, v95, v37
	v_fma_f32 v22, -v36, v94, v22
	v_div_fmas_f32 v22, v22, v37, v94
	v_div_fixup_f32 v22, v22, v23, 1.0
	v_pk_mul_f32 v[36:37], v[100:101], v[22:23] op_sel_hi:[1,0]
	v_pk_mul_f32 v[44:45], v[44:45], v[22:23] op_sel_hi:[1,0]
	s_waitcnt vmcnt(0)
; __device__ __forceinline__ unsigned pk2(float lo, float hi) { const f32x2_t v = {lo, hi}; return __builtin_bit_cast(unsigned, __builtin_convertvector(v, bf16x2_t)); }
; __device__ __forceinline__ float sigmoidf_(float x) { return __builtin_amdgcn_rcpf(1.0f + __expf(-x)); }
; __device__ __forceinline__ void mlstm_out_group(Frame& F, int l, int ug) {
;     ...
;             for (int mt = 0; mt < 8; ++mt) { const int v = 16 * mt + 4 * g;
;                 const f32x4 go4 = *(const f32x4*)(gout + v); const v2u mx = mx8[mt];
;                 v2u wv; wv.x = pk2(o[mt][0] * rstd * go4.x * sigmoidf_(bflo(mx.x)), o[mt][1] * rstd * go4.y * sigmoidf_(bfhi(mx.x))); wv.y = pk2(o[mt][2] * rstd * go4.z * sigmoidf_(bflo(mx.y)), o[mt][3] * rstd * go4.w * sigmoidf_(bfhi(mx.y)));
;                 *(v2u*)(Y + row * DM + h * 128 + v) = wv; }
	v_pk_mul_f32 v[36:37], v[46:47], v[36:37]
	v_pk_mul_f32 v[44:45], v[48:49], v[44:45]
	v_pk_mul_f32 v[36:37], v[92:93], v[36:37]
	v_pk_mul_f32 v[26:27], v[26:27], v[44:45]
	v_cvt_pk_bf16_f32 v36, v36, v37
	v_cvt_pk_bf16_f32 v37, v26, v27
	global_load_dwordx4 v[44:47], v[90:91], off offset:64
	global_store_dwordx2 v[18:19], v[36:37], off
	v_lshlrev_b32_e32 v23, 16, v114
	v_mul_f32_e32 v23, 0xbfb8aa3b, v23
	v_and_b32_e32 v26, 0xffff0000, v114
	v_exp_f32_e32 v23, v23
	v_mul_f32_e32 v26, 0xbfb8aa3b, v26
	v_exp_f32_e32 v27, v26
	s_andn2_b64 vcc, exec, s[60:61]
	v_add_f32_e32 v23, 1.0, v23
	v_rcp_f32_e32 v26, v23
	v_add_f32_e32 v23, 1.0, v27
	v_lshlrev_b32_e32 v27, 16, v115
	v_mul_f32_e32 v27, 0xbfb8aa3b, v27
	v_exp_f32_e32 v36, v27
	v_and_b32_e32 v27, 0xffff0000, v115
	v_mul_f32_e32 v27, 0xbfb8aa3b, v27
	v_exp_f32_e32 v37, v27
	v_rcp_f32_e32 v27, v23
	v_add_f32_e32 v23, 1.0, v36
	v_rcp_f32_e32 v36, v23
	v_add_f32_e32 v23, 1.0, v37
	v_rcp_f32_e32 v37, v23
	v_pk_mul_f32 v[48:49], v[184:185], v[22:23] op_sel_hi:[1,0]
	s_waitcnt vmcnt(1) lgkmcnt(0)
	v_pk_mul_f32 v[44:45], v[44:45], v[48:49]
	s_nop 0
	v_pk_mul_f32 v[26:27], v[26:27], v[44:45]
	v_pk_mul_f32 v[44:45], v[96:97], v[22:23] op_sel_hi:[1,0]
	v_cvt_pk_bf16_f32 v26, v26, v27
	v_pk_mul_f32 v[44:45], v[46:47], v[44:45]
	v_lshlrev_b32_e32 v23, 16, v112
	v_pk_mul_f32 v[36:37], v[36:37], v[44:45]
	v_mul_f32_e32 v23, 0xbfb8aa3b, v23
	v_cvt_pk_bf16_f32 v27, v36, v37
	global_load_dwordx4 v[44:47], v[90:91], off offset:128
	global_store_dwordx2 v[18:19], v[26:27], off offset:32
	v_and_b32_e32 v26, 0xffff0000, v112
	v_lshlrev_b32_e32 v27, 16, v113
	v_and_b32_e32 v36, 0xffff0000, v113
	v_mul_f32_e32 v26, 0xbfb8aa3b, v26
	v_mul_f32_e32 v27, 0xbfb8aa3b, v27
	v_mul_f32_e32 v36, 0xbfb8aa3b, v36
	v_exp_f32_e32 v23, v23
	v_exp_f32_e32 v26, v26
	v_exp_f32_e32 v27, v27
	v_exp_f32_e32 v36, v36
	v_add_f32_e32 v23, 1.0, v23
	v_add_f32_e32 v37, 1.0, v26
	v_add_f32_e32 v48, 1.0, v27
	v_add_f32_e32 v49, 1.0, v36
	v_rcp_f32_e32 v26, v23
	v_rcp_f32_e32 v27, v37
	v_rcp_f32_e32 v36, v48
	v_rcp_f32_e32 v37, v49
	v_pk_mul_f32 v[48:49], v[98:99], v[22:23] op_sel_hi:[1,0]
	v_pk_mul_f32 v[42:43], v[42:43], v[22:23] op_sel_hi:[1,0]
	v_lshlrev_b32_e32 v23, 16, v110
	v_mul_f32_e32 v23, 0xbfb8aa3b, v23
	v_exp_f32_e32 v23, v23
	s_waitcnt vmcnt(1) lgkmcnt(0)
	v_pk_mul_f32 v[44:45], v[44:45], v[48:49]
	v_pk_mul_f32 v[42:43], v[46:47], v[42:43]
	v_pk_mul_f32 v[26:27], v[26:27], v[44:45]
	v_pk_mul_f32 v[36:37], v[36:37], v[42:43]
	v_cvt_pk_bf16_f32 v26, v26, v27
	v_cvt_pk_bf16_f32 v27, v36, v37
	global_load_dwordx4 v[42:45], v[90:91], off offset:192
	global_store_dwordx2 v[18:19], v[26:27], off offset:64
	v_and_b32_e32 v26, 0xffff0000, v110
	v_lshlrev_b32_e32 v27, 16, v111
	v_and_b32_e32 v36, 0xffff0000, v111
	v_mul_f32_e32 v26, 0xbfb8aa3b, v26
	v_mul_f32_e32 v27, 0xbfb8aa3b, v27
	v_mul_f32_e32 v36, 0xbfb8aa3b, v36
	v_exp_f32_e32 v26, v26
	v_exp_f32_e32 v27, v27
	v_exp_f32_e32 v36, v36
	v_add_f32_e32 v23, 1.0, v23
	v_add_f32_e32 v37, 1.0, v26
	v_add_f32_e32 v46, 1.0, v27
	v_add_f32_e32 v47, 1.0, v36
	v_rcp_f32_e32 v26, v23
	v_rcp_f32_e32 v27, v37
	v_rcp_f32_e32 v36, v46
	v_rcp_f32_e32 v37, v47
	v_pk_mul_f32 v[40:41], v[40:41], v[22:23] op_sel_hi:[1,0]
	v_pk_mul_f32 v[38:39], v[38:39], v[22:23] op_sel_hi:[1,0]
	v_lshlrev_b32_e32 v23, 16, v108
	v_mul_f32_e32 v23, 0xbfb8aa3b, v23
	v_exp_f32_e32 v23, v23
	s_waitcnt vmcnt(1) lgkmcnt(0)
	v_pk_mul_f32 v[40:41], v[42:43], v[40:41]
	v_pk_mul_f32 v[38:39], v[44:45], v[38:39]
	v_pk_mul_f32 v[26:27], v[26:27], v[40:41]
	v_pk_mul_f32 v[36:37], v[36:37], v[38:39]
	v_cvt_pk_bf16_f32 v26, v26, v27
	v_cvt_pk_bf16_f32 v27, v36, v37
	global_load_dwordx4 v[36:39], v[90:91], off offset:256
	global_store_dwordx2 v[18:19], v[26:27], off offset:96
	v_and_b32_e32 v26, 0xffff0000, v108
	v_lshlrev_b32_e32 v27, 16, v109
	v_and_b32_e32 v40, 0xffff0000, v109
	v_mul_f32_e32 v26, 0xbfb8aa3b, v26
	v_mul_f32_e32 v27, 0xbfb8aa3b, v27
	v_mul_f32_e32 v40, 0xbfb8aa3b, v40
	v_exp_f32_e32 v26, v26
	v_exp_f32_e32 v27, v27
	v_exp_f32_e32 v40, v40
	v_add_f32_e32 v23, 1.0, v23
	v_add_f32_e32 v41, 1.0, v26
	v_add_f32_e32 v42, 1.0, v27
	v_add_f32_e32 v43, 1.0, v40
	v_rcp_f32_e32 v26, v23
	v_rcp_f32_e32 v27, v41
	v_rcp_f32_e32 v40, v42
	v_rcp_f32_e32 v41, v43
	v_pk_mul_f32 v[34:35], v[34:35], v[22:23] op_sel_hi:[1,0]
	v_pk_mul_f32 v[32:33], v[32:33], v[22:23] op_sel_hi:[1,0]
	v_lshlrev_b32_e32 v23, 16, v106
	v_mul_f32_e32 v23, 0xbfb8aa3b, v23
	v_exp_f32_e32 v23, v23
	s_waitcnt vmcnt(1) lgkmcnt(0)
; __device__ __forceinline__ unsigned pk2(float lo, float hi) { const f32x2_t v = {lo, hi}; return __builtin_bit_cast(unsigned, __builtin_convertvector(v, bf16x2_t)); }
; __device__ __forceinline__ float sigmoidf_(float x) { return __builtin_amdgcn_rcpf(1.0f + __expf(-x)); }
; __device__ __forceinline__ void mlstm_out_group(Frame& F, int l, int ug) {
;     ...
;             for (int mt = 0; mt < 8; ++mt) { const int v = 16 * mt + 4 * g;
;                 const f32x4 go4 = *(const f32x4*)(gout + v); const v2u mx = mx8[mt];
;                 v2u wv; wv.x = pk2(o[mt][0] * rstd * go4.x * sigmoidf_(bflo(mx.x)), o[mt][1] * rstd * go4.y * sigmoidf_(bfhi(mx.x))); wv.y = pk2(o[mt][2] * rstd * go4.z * sigmoidf_(bflo(mx.y)), o[mt][3] * rstd * go4.w * sigmoidf_(bfhi(mx.y)));
;                 *(v2u*)(Y + row * DM + h * 128 + v) = wv; }
	v_pk_mul_f32 v[34:35], v[36:37], v[34:35]
	v_pk_mul_f32 v[32:33], v[38:39], v[32:33]
	v_pk_mul_f32 v[26:27], v[26:27], v[34:35]
	v_pk_mul_f32 v[32:33], v[40:41], v[32:33]
	v_cvt_pk_bf16_f32 v26, v26, v27
	v_cvt_pk_bf16_f32 v27, v32, v33
	global_load_dwordx4 v[32:35], v[90:91], off offset:320
	global_store_dwordx2 v[18:19], v[26:27], off offset:128
	v_and_b32_e32 v26, 0xffff0000, v106
	v_lshlrev_b32_e32 v27, 16, v107
	v_and_b32_e32 v36, 0xffff0000, v107
	v_mul_f32_e32 v26, 0xbfb8aa3b, v26
	v_mul_f32_e32 v27, 0xbfb8aa3b, v27
	v_mul_f32_e32 v36, 0xbfb8aa3b, v36
	v_exp_f32_e32 v26, v26
	v_exp_f32_e32 v27, v27
	v_exp_f32_e32 v36, v36
	v_add_f32_e32 v23, 1.0, v23
	v_add_f32_e32 v37, 1.0, v26
	v_add_f32_e32 v38, 1.0, v27
	v_add_f32_e32 v39, 1.0, v36
	v_rcp_f32_e32 v26, v23
	v_rcp_f32_e32 v27, v37
	v_rcp_f32_e32 v36, v38
	v_rcp_f32_e32 v37, v39
	v_pk_mul_f32 v[30:31], v[30:31], v[22:23] op_sel_hi:[1,0]
	v_pk_mul_f32 v[24:25], v[24:25], v[22:23] op_sel_hi:[1,0]
	v_lshlrev_b32_e32 v23, 16, v104
	v_mul_f32_e32 v23, 0xbfb8aa3b, v23
	v_exp_f32_e32 v23, v23
	s_waitcnt vmcnt(1) lgkmcnt(0)
	v_pk_mul_f32 v[30:31], v[32:33], v[30:31]
	v_pk_mul_f32 v[24:25], v[34:35], v[24:25]
	v_pk_mul_f32 v[26:27], v[26:27], v[30:31]
	v_pk_mul_f32 v[24:25], v[36:37], v[24:25]
	v_cvt_pk_bf16_f32 v26, v26, v27
	v_cvt_pk_bf16_f32 v27, v24, v25
	global_store_dwordx2 v[18:19], v[26:27], off offset:160
	global_load_dwordx4 v[24:27], v[90:91], off offset:384
	v_and_b32_e32 v30, 0xffff0000, v104
	v_lshlrev_b32_e32 v31, 16, v105
	v_and_b32_e32 v32, 0xffff0000, v105
	v_mul_f32_e32 v30, 0xbfb8aa3b, v30
	v_mul_f32_e32 v31, 0xbfb8aa3b, v31
	v_mul_f32_e32 v32, 0xbfb8aa3b, v32
	v_exp_f32_e32 v30, v30
	v_exp_f32_e32 v31, v31
	v_exp_f32_e32 v32, v32
	v_add_f32_e32 v23, 1.0, v23
	v_add_f32_e32 v33, 1.0, v30
	v_add_f32_e32 v34, 1.0, v31
	v_add_f32_e32 v35, 1.0, v32
	v_rcp_f32_e32 v30, v23
	v_rcp_f32_e32 v31, v33
	v_rcp_f32_e32 v32, v34
	v_rcp_f32_e32 v33, v35
	v_pk_mul_f32 v[20:21], v[20:21], v[22:23] op_sel_hi:[1,0]
	v_pk_mul_f32 v[34:35], v[88:89], v[22:23] op_sel_hi:[1,0]
	v_lshlrev_b32_e32 v23, 16, v103
	v_mul_f32_e32 v23, 0xbfb8aa3b, v23
	v_exp_f32_e32 v23, v23
	s_waitcnt vmcnt(0) lgkmcnt(0)
	v_pk_mul_f32 v[20:21], v[24:25], v[20:21]
	v_pk_mul_f32 v[24:25], v[26:27], v[34:35]
	v_pk_mul_f32 v[20:21], v[30:31], v[20:21]
	v_pk_mul_f32 v[24:25], v[32:33], v[24:25]
	v_cvt_pk_bf16_f32 v20, v20, v21
	v_cvt_pk_bf16_f32 v21, v24, v25
	global_load_dwordx4 v[24:27], v[90:91], off offset:448
	global_store_dwordx2 v[18:19], v[20:21], off offset:192
	v_lshlrev_b32_e32 v20, 16, v102
	v_and_b32_e32 v21, 0xffff0000, v102
	v_and_b32_e32 v30, 0xffff0000, v103
	v_mul_f32_e32 v20, 0xbfb8aa3b, v20
	v_mul_f32_e32 v21, 0xbfb8aa3b, v21
	v_mul_f32_e32 v30, 0xbfb8aa3b, v30
	v_exp_f32_e32 v20, v20
	v_exp_f32_e32 v21, v21
	v_exp_f32_e32 v30, v30
	v_add_f32_e32 v23, 1.0, v23
	v_add_f32_e32 v20, 1.0, v20
	v_add_f32_e32 v21, 1.0, v21
	v_add_f32_e32 v31, 1.0, v30
	v_rcp_f32_e32 v20, v20
	v_rcp_f32_e32 v21, v21
	v_rcp_f32_e32 v30, v23
	v_rcp_f32_e32 v31, v31
	v_pk_mul_f32 v[28:29], v[28:29], v[22:23] op_sel_hi:[1,0]
	v_pk_mul_f32 v[22:23], v[86:87], v[22:23] op_sel_hi:[1,0]
	s_waitcnt vmcnt(1) lgkmcnt(0)
	v_pk_mul_f32 v[24:25], v[24:25], v[28:29]
	v_pk_mul_f32 v[22:23], v[26:27], v[22:23]
	v_pk_mul_f32 v[20:21], v[20:21], v[24:25]
	v_pk_mul_f32 v[22:23], v[30:31], v[22:23]
	v_cvt_pk_bf16_f32 v20, v20, v21
	v_cvt_pk_bf16_f32 v21, v22, v23
	global_store_dwordx2 v[18:19], v[20:21], off offset:224
	s_cbranch_vccz .LBB0_1287
